# MoBA item prologue de-serialised: K/V tile loads issued together into separate registers with counted waits (was six serial load+wait round trips per item)
# speedup vs baseline: 1.0173x; 1.0012x over previous
.LBB0_654:
	s_or_b64 exec, exec, s[0:1]
	s_ashr_i32 s0, s11, 5
	s_and_b32 s0, s0, -8
	s_lshr_b32 s16, s14, s0
	s_and_b32 s0, s11, 31
	s_and_b32 s28, s16, 31
	s_and_b32 s27, s11, 15
	s_lshl_b32 s0, s0, 15
	s_add_u32 s14, s2, s0
	s_addc_u32 s15, s3, 0
	s_lshl_b32 s29, s28, 8
	v_add_u32_e32 v15, s29, v162
	s_movk_i32 s17, 0x2000
	v_cmp_gt_i32_e32 vcc, s17, v15
	v_add_u32_e32 v0, 0x200, v15
	v_cmp_gt_i32_e64 s[0:1], s17, v0
	v_cndmask_b32_e32 v2, 0, v15, vcc
	v_ashrrev_i32_e32 v3, 31, v2
	v_lshl_add_u64 v[2:3], v[2:3], 2, s[14:15]
	global_load_dword v33, v[2:3], off
	v_cndmask_b32_e64 v2, 0, v0, s[0:1]
	v_ashrrev_i32_e32 v3, 31, v2
	v_add_u32_e32 v0, 0x400, v15
	v_lshl_add_u64 v[2:3], v[2:3], 2, s[14:15]
	v_cmp_gt_i32_e64 s[0:1], s17, v0
	global_load_dword v32, v[2:3], off
	v_mov_b32_e32 v155, v1
	v_cndmask_b32_e64 v2, 0, v0, s[0:1]
	v_ashrrev_i32_e32 v3, 31, v2
	v_add_u32_e32 v0, 0x600, v15
	v_lshl_add_u64 v[2:3], v[2:3], 2, s[14:15]
	v_cmp_gt_i32_e64 s[0:1], s17, v0
	global_load_dword v14, v[2:3], off
	s_nop 0
	v_cndmask_b32_e64 v2, 0, v0, s[0:1]
	v_ashrrev_i32_e32 v3, 31, v2
	v_add_u32_e32 v0, 0x800, v15
	v_lshl_add_u64 v[2:3], v[2:3], 2, s[14:15]
	v_cmp_gt_i32_e64 s[0:1], s17, v0
	global_load_dword v13, v[2:3], off
	s_nop 0
	v_cndmask_b32_e64 v2, 0, v0, s[0:1]
	v_ashrrev_i32_e32 v3, 31, v2
	v_add_u32_e32 v0, 0xa00, v15
	v_lshl_add_u64 v[2:3], v[2:3], 2, s[14:15]
	v_cmp_gt_i32_e64 s[0:1], s17, v0
	global_load_dword v12, v[2:3], off
	s_nop 0
	v_cndmask_b32_e64 v2, 0, v0, s[0:1]
	v_ashrrev_i32_e32 v3, 31, v2
	v_add_u32_e32 v0, 0xc00, v15
	v_lshl_add_u64 v[2:3], v[2:3], 2, s[14:15]
	v_cmp_gt_i32_e64 s[0:1], s17, v0
	global_load_dword v11, v[2:3], off
	s_nop 0
	v_cndmask_b32_e64 v2, 0, v0, s[0:1]
	v_ashrrev_i32_e32 v3, 31, v2
	v_add_u32_e32 v0, 0xe00, v15
	v_lshl_add_u64 v[2:3], v[2:3], 2, s[14:15]
	v_cmp_gt_i32_e64 s[0:1], s17, v0
	global_load_dword v10, v[2:3], off
	s_nop 0
	v_cndmask_b32_e64 v2, 0, v0, s[0:1]
	v_ashrrev_i32_e32 v3, 31, v2
	v_add_u32_e32 v0, 0x1000, v15
	v_lshl_add_u64 v[2:3], v[2:3], 2, s[14:15]
	v_cmp_gt_i32_e64 s[0:1], s17, v0
	global_load_dword v9, v[2:3], off
	s_nop 0
	v_cndmask_b32_e64 v2, 0, v0, s[0:1]
	v_ashrrev_i32_e32 v3, 31, v2
	v_add_u32_e32 v0, 0x1200, v15
	v_lshl_add_u64 v[2:3], v[2:3], 2, s[14:15]
	v_cmp_gt_i32_e64 s[0:1], s17, v0
	global_load_dword v8, v[2:3], off
	s_nop 0
	v_cndmask_b32_e64 v2, 0, v0, s[0:1]
	v_ashrrev_i32_e32 v3, 31, v2
	v_add_u32_e32 v0, 0x1400, v15
	v_lshl_add_u64 v[2:3], v[2:3], 2, s[14:15]
	v_cmp_gt_i32_e64 s[0:1], s17, v0
	global_load_dword v7, v[2:3], off
	s_nop 0
	v_cndmask_b32_e64 v2, 0, v0, s[0:1]
	v_ashrrev_i32_e32 v3, 31, v2
	v_add_u32_e32 v0, 0x1600, v15
	v_lshl_add_u64 v[2:3], v[2:3], 2, s[14:15]
	v_cmp_gt_i32_e64 s[0:1], s17, v0
	global_load_dword v6, v[2:3], off
	s_nop 0
	v_cndmask_b32_e64 v2, 0, v0, s[0:1]
	v_ashrrev_i32_e32 v3, 31, v2
	v_add_u32_e32 v0, 0x1800, v15
	v_lshl_add_u64 v[2:3], v[2:3], 2, s[14:15]
	v_cmp_gt_i32_e64 s[0:1], s17, v0
	global_load_dword v5, v[2:3], off
	s_nop 0
	v_cndmask_b32_e64 v2, 0, v0, s[0:1]
	v_ashrrev_i32_e32 v3, 31, v2
	v_add_u32_e32 v0, 0x1a00, v15
	v_lshl_add_u64 v[2:3], v[2:3], 2, s[14:15]
	v_cmp_gt_i32_e64 s[0:1], s17, v0
	global_load_dword v4, v[2:3], off
	s_nop 0
	v_cndmask_b32_e64 v2, 0, v0, s[0:1]
	v_add_u32_e32 v0, 0x1c00, v15
	v_cmp_gt_i32_e64 s[0:1], s17, v0
	v_ashrrev_i32_e32 v3, 31, v2
	v_lshl_add_u64 v[2:3], v[2:3], 2, s[14:15]
	v_cndmask_b32_e64 v34, 0, v0, s[0:1]
	v_ashrrev_i32_e32 v35, 31, v34
	v_add_u32_e32 v0, 0x1e00, v15
	v_lshl_add_u64 v[34:35], v[34:35], 2, s[14:15]
	v_cmp_gt_i32_e64 s[0:1], s17, v0
	global_load_dword v3, v[2:3], off
	s_nop 0
	global_load_dword v2, v[34:35], off
	v_cndmask_b32_e64 v34, 0, v0, s[0:1]
	s_lshl_b32 s0, s11, 9
	s_and_b32 s26, s0, 0x2000
	s_or_b32 s0, s29, s26
	s_mulk_i32 s0, 0x1800
	s_add_u32 s0, s8, s0
	s_addc_u32 s1, s9, 0
	s_lshl_b32 s17, s27, 7
	s_add_u32 s0, s0, s17
	s_addc_u32 s1, s1, 0
	v_lshl_add_u64 v[38:39], s[0:1], 0, v[154:155]
	s_mov_b64 s[0:1], 0x1000
	v_ashrrev_i32_e32 v35, 31, v34
	v_lshl_add_u64 v[46:47], v[38:39], 0, s[0:1]
	v_lshl_add_u64 v[34:35], v[34:35], 2, s[14:15]
	v_lshl_add_u64 v[42:43], v[46:47], 0, v[148:149]
	global_load_dword v0, v[34:35], off
	s_mov_b32 s0, 0x5040100
	global_load_dwordx4 v[42:45], v[42:43], off
	v_lshl_add_u64 v[34:35], v[38:39], 0, v[136:137]
	global_load_dwordx4 v[34:37], v[34:35], off offset:2048
	v_lshl_add_u64 v[216:217], v[38:39], 0, v[138:139]
	global_load_dwordx4 v[200:203], v[216:217], off offset:2048
	v_lshl_add_u64 v[218:219], v[38:39], 0, v[140:141]
	global_load_dwordx4 v[204:207], v[218:219], off offset:2048
	v_lshl_add_u64 v[216:217], v[38:39], 0, v[142:143]
	global_load_dwordx4 v[208:211], v[216:217], off offset:2048
	v_lshl_add_u64 v[38:39], v[46:47], 0, v[146:147]
	global_load_dwordx4 v[38:41], v[38:39], off
	v_lshl_add_u64 v[218:219], v[46:47], 0, v[144:145]
	v_lshl_add_u64 v[46:47], v[46:47], 0, v[150:151]
	global_load_dwordx4 v[212:215], v[218:219], off
	global_load_dwordx4 v[46:49], v[46:47], off
	s_mov_b32 s1, 0x7060302
	s_lshl_b32 s33, 1, s16
	s_cmp_eq_u32 s28, 31
	s_waitcnt vmcnt(6)
	ds_write_b128 v184, v[34:37]
	s_waitcnt vmcnt(5)
	ds_write_b128 v185, v[200:203]
	s_waitcnt vmcnt(4)
	ds_write_b128 v186, v[204:207]
	s_waitcnt vmcnt(3)
	ds_write_b128 v187, v[208:211]
	s_waitcnt vmcnt(0)
	v_perm_b32 v50, v38, v212, s0
	v_perm_b32 v52, v38, v212, s1
	v_perm_b32 v34, v39, v213, s1
	v_perm_b32 v38, v40, v214, s1
	v_perm_b32 v51, v46, v42, s0
	v_perm_b32 v53, v46, v42, s1
	ds_write_b64 v188, v[50:51] offset:36864
	ds_write_b64 v189, v[52:53] offset:36864
	v_perm_b32 v50, v39, v213, s0
	v_perm_b32 v51, v47, v43, s0
	v_perm_b32 v35, v47, v43, s1
	ds_write_b64 v190, v[50:51] offset:36864
	ds_write_b64 v191, v[34:35] offset:36864
	v_perm_b32 v34, v40, v214, s0
	v_perm_b32 v35, v48, v44, s0
	v_perm_b32 v39, v48, v44, s1
	ds_write_b64 v192, v[34:35] offset:36864
	ds_write_b64 v193, v[38:39] offset:36864
	v_perm_b32 v34, v41, v215, s0
	v_perm_b32 v35, v49, v45, s0
	v_perm_b32 v36, v41, v215, s1
	v_perm_b32 v37, v49, v45, s1
	ds_write_b64 v194, v[34:35] offset:36864
	ds_write_b64 v195, v[36:37] offset:36864
	s_waitcnt lgkmcnt(0)
	s_barrier
	s_cbranch_scc1 .LBB0_718
	v_and_b32_e32 v34, s33, v33
	v_cmp_ne_u32_e64 s[0:1], 0, v34
	s_and_b64 s[16:17], vcc, s[0:1]
	v_cndmask_b32_e64 v34, 0, 1, s[16:17]
	v_cmp_ne_u32_e32 vcc, 0, v34
	s_cmp_lg_u64 vcc, 0
	s_cselect_b64 s[0:1], -1, 0
	v_mov_b32_e32 v33, 0
	s_and_b64 s[0:1], s[42:43], s[0:1]
	s_and_saveexec_b64 s[18:19], s[0:1]
	s_cbranch_execz .LBB0_659
	s_mov_b64 s[34:35], exec
	v_mbcnt_lo_u32_b32 v33, s34, 0
	v_mbcnt_hi_u32_b32 v33, s35, v33
	s_bcnt1_i32_b64 s25, vcc
	v_cmp_eq_u32_e64 s[0:1], 0, v33
	s_and_saveexec_b64 s[30:31], s[0:1]
	s_cbranch_execz .LBB0_658
	s_bcnt1_i32_b64 s0, s[34:35]
	s_mul_i32 s0, s25, s0
	v_readlane_b32 s1, v254, 48
	v_mov_b32_e32 v35, s0
	s_nop 0
	v_mov_b32_e32 v34, s1
	ds_add_rtn_u32 v34, v34, v35
